# SwiGLU epilogue activation stores with default cache policy instead of nt (dense and expert gate/up GEMMs)
# speedup vs baseline: 1.0066x; 1.0066x over previous
; __device__ __forceinline__ unsigned cvt_pk4_fp8(float a, float b, float c, float d) { int w = 0; w = __builtin_amdgcn_cvt_pk_fp8_f32(a, b, w, false); w = __builtin_amdgcn_cvt_pk_fp8_f32(c, d, w, true); return (unsigned)w; }
; __device__ __forceinline__ unsigned cvt_pk_bf16(float lo, float hi) { unsigned r; asm volatile("v_cvt_pk_bf16_f32 %0, %1, %2" : "=v"(r) : "v"(lo), "v"(hi)); return r; }
; __device__ __forceinline__ f32x2p silu_mul2k(f32x2p ag, f32x2p au, float kt, float ci) { const f32x2p t = ag * kt; f32x2p e; e.x = __builtin_amdgcn_exp2f(t.x); e.y = __builtin_amdgcn_exp2f(t.y);
;     const f32x2p d = e * ci + ci; f32x2p r; r.x = __builtin_amdgcn_rcpf(d.x); r.y = __builtin_amdgcn_rcpf(d.y); return (ag * au) * r; }
;     __device__ __forceinline__ void operator()(const f32x4 (&acc)[2][2][4][2], const Unit& u, int wr, int wc, int fr, int fq) const {
;         const int row0 = u.orow + wr * 64 + fr, col0 = u.ocol * HALF + wc * 32 + 8 * fq;
;         const float kt = -1.4426950408889634f * sc, ci = 1.f / (sc * sc * oscale);
; #pragma unroll
;         for (int ai = 0; ai < 2; ++ai)
; #pragma unroll
;             for (int m = 0; m < 4; ++m) { const size_t off = (size_t)(row0 + ai * HALF + m * 16) * ldc + col0;
;                 const f32x4 g0 = acc[ai][0][m][0], g1 = acc[ai][0][m][1], u0 = acc[ai][1][m][0], u1 = acc[ai][1][m][1];
;                 float v[8];
;                 { const f32x2p a = silu_mul2k((f32x2p){g0[0], g0[1]}, (f32x2p){u0[0], u0[1]}, kt, ci), b = silu_mul2k((f32x2p){g0[2], g0[3]}, (f32x2p){u0[2], u0[3]}, kt, ci), c = silu_mul2k((f32x2p){g1[0], g1[1]}, (f32x2p){u1[0], u1[1]}, kt, ci), d = silu_mul2k((f32x2p){g1[2], g1[3]}, (f32x2p){u1[2], u1[3]}, kt, ci);
;                   v[0] = a.x; v[1] = a.y; v[2] = b.x; v[3] = b.y; v[4] = c.x; v[5] = c.y; v[6] = d.x; v[7] = d.y; }
;                 if constexpr (FP8OUT) { typedef unsigned u32x2 __attribute__((ext_vector_type(2))); u32x2 w; w.x = cvt_pk4_fp8(v[0], v[1], v[2], v[3]); w.y = cvt_pk4_fp8(v[4], v[5], v[6], v[7]); __builtin_nontemporal_store(w, (u32x2*)((unsigned char*)O + off)); }
;                 else { u32x4 w; w.x = cvt_pk_bf16(v[0], v[1]); w.y = cvt_pk_bf16(v[2], v[3]); w.z = cvt_pk_bf16(v[4], v[5]); w.w = cvt_pk_bf16(v[6], v[7]); __builtin_nontemporal_store(w, (u32x4*)((bf16_t*)O + off)); } }
.LBB0_870:
	v_pk_mul_f32 v[0:1], v[156:157], s[16:17] op_sel_hi:[1,0]
	v_pk_mul_f32 v[8:9], v[156:157], v[124:125]
	v_exp_f32_e32 v2, v0
	v_exp_f32_e32 v3, v1
	v_pk_mul_f32 v[10:11], v[152:153], s[16:17] op_sel_hi:[1,0]
	v_pk_mul_f32 v[12:13], v[154:155], s[16:17] op_sel_hi:[1,0]
	v_exp_f32_e32 v10, v10
	v_pk_fma_f32 v[2:3], v[2:3], s[22:23], s[22:23] op_sel_hi:[1,0,0]
	v_exp_f32_e32 v11, v11
	v_rcp_f32_e32 v2, v2
	v_rcp_f32_e32 v3, v3
	v_exp_f32_e32 v12, v12
	v_pk_fma_f32 v[10:11], v[10:11], s[22:23], s[22:23] op_sel_hi:[1,0,0]
	v_exp_f32_e32 v13, v13
	v_pk_mul_f32 v[2:3], v[8:9], v[2:3]
	v_pk_mul_f32 v[8:9], v[158:159], s[16:17] op_sel_hi:[1,0]
	v_rcp_f32_e32 v10, v10
	v_exp_f32_e32 v8, v8
	v_exp_f32_e32 v9, v9
	v_rcp_f32_e32 v11, v11
	v_pk_mul_f32 v[6:7], v[158:159], v[126:127]
	v_add_u32_e32 v4, s61, v184
	v_pk_fma_f32 v[8:9], v[8:9], s[22:23], s[22:23] op_sel_hi:[1,0,0]
	v_lshl_add_u32 v0, s62, 7, v186
	v_rcp_f32_e32 v8, v8
	v_rcp_f32_e32 v9, v9
	v_ashrrev_i32_e32 v1, 31, v0
	s_nop 15
	s_nop 15
	v_pk_mul_f32 v[14:15], v[146:147], s[16:17] op_sel_hi:[1,0]
	v_pk_mul_f32 v[6:7], v[6:7], v[8:9]
	v_pk_mul_f32 v[8:9], v[152:153], v[120:121]
	v_exp_f32_e32 v14, v14
	v_pk_mul_f32 v[8:9], v[8:9], v[10:11]
	v_pk_fma_f32 v[10:11], v[12:13], s[22:23], s[22:23] op_sel_hi:[1,0,0]
	v_mov_b32_e32 v12, 0
	v_cvt_pk_fp8_f32 v12, v2, v3
	v_rcp_f32_e32 v10, v10
	v_rcp_f32_e32 v11, v11
	v_mov_b32_e32 v13, 0
	v_cvt_pk_fp8_f32 v12, v6, v7 op_sel:[0,0,1]
	v_pk_mul_f32 v[6:7], v[148:149], s[16:17] op_sel_hi:[1,0]
	v_cvt_pk_fp8_f32 v13, v8, v9
	v_exp_f32_e32 v6, v6
	v_exp_f32_e32 v7, v7
	v_pk_mul_f32 v[2:3], v[154:155], v[122:123]
	v_exp_f32_e32 v15, v15
	v_pk_mul_f32 v[2:3], v[2:3], v[10:11]
	v_pk_fma_f32 v[6:7], v[6:7], s[22:23], s[22:23] op_sel_hi:[1,0,0]
	v_cvt_pk_fp8_f32 v13, v2, v3 op_sel:[0,0,1]
	v_rcp_f32_e32 v6, v6
	v_rcp_f32_e32 v7, v7
	v_mov_b64_e32 v[2:3], s[20:21]
	v_mad_i64_i32 v[8:9], s[44:45], v4, s58, v[2:3]
	v_pk_mul_f32 v[10:11], v[148:149], v[116:117]
	v_lshl_add_u64 v[8:9], v[8:9], 0, v[0:1]
	v_pk_mul_f32 v[6:7], v[10:11], v[6:7]
	v_pk_mul_f32 v[10:11], v[150:151], s[16:17] op_sel_hi:[1,0]
	global_store_dwordx2 v[8:9], v[12:13], off
	v_exp_f32_e32 v10, v10
	v_exp_f32_e32 v11, v11
	v_pk_mul_f32 v[12:13], v[144:145], s[16:17] op_sel_hi:[1,0]
	v_pk_mul_f32 v[8:9], v[150:151], v[118:119]
	v_exp_f32_e32 v12, v12
	v_exp_f32_e32 v13, v13
	v_pk_fma_f32 v[10:11], v[10:11], s[22:23], s[22:23] op_sel_hi:[1,0,0]
	v_add_u32_e32 v5, 16, v4
	v_rcp_f32_e32 v10, v10
	v_rcp_f32_e32 v11, v11
	v_pk_fma_f32 v[12:13], v[12:13], s[22:23], s[22:23] op_sel_hi:[1,0,0]
	v_readlane_b32 s68, v254, 28
	v_rcp_f32_e32 v12, v12
	v_rcp_f32_e32 v13, v13
	v_pk_mul_f32 v[8:9], v[8:9], v[10:11]
	v_pk_mul_f32 v[10:11], v[144:145], v[112:113]
	s_andn2_b64 vcc, exec, s[8:9]
	v_pk_mul_f32 v[10:11], v[10:11], v[12:13]
	v_pk_fma_f32 v[12:13], v[14:15], s[22:23], s[22:23] op_sel_hi:[1,0,0]
	v_mov_b32_e32 v15, 0
	v_rcp_f32_e32 v12, v12
	v_rcp_f32_e32 v13, v13
	v_cvt_pk_fp8_f32 v15, v10, v11
	v_mov_b32_e32 v14, 0
	v_cvt_pk_fp8_f32 v14, v6, v7
	v_pk_mul_f32 v[6:7], v[146:147], v[114:115]
	v_pk_mul_f32 v[10:11], v[140:141], v[108:109]
	v_pk_mul_f32 v[6:7], v[6:7], v[12:13]
	v_pk_mul_f32 v[12:13], v[136:137], s[16:17] op_sel_hi:[1,0]
	v_cvt_pk_fp8_f32 v15, v6, v7 op_sel:[0,0,1]
	v_pk_mul_f32 v[6:7], v[140:141], s[16:17] op_sel_hi:[1,0]
	v_cvt_pk_fp8_f32 v14, v8, v9 op_sel:[0,0,1]
	v_exp_f32_e32 v6, v6
	v_exp_f32_e32 v7, v7
	v_exp_f32_e32 v12, v12
	v_exp_f32_e32 v13, v13
	v_mad_i64_i32 v[8:9], s[44:45], v5, s58, v[2:3]
	v_pk_fma_f32 v[6:7], v[6:7], s[22:23], s[22:23] op_sel_hi:[1,0,0]
	v_lshl_add_u64 v[8:9], v[8:9], 0, v[0:1]
	v_rcp_f32_e32 v6, v6
	v_rcp_f32_e32 v7, v7
	global_store_dwordx2 v[8:9], v[14:15], off
	v_pk_fma_f32 v[12:13], v[12:13], s[22:23], s[22:23] op_sel_hi:[1,0,0]
	v_pk_mul_f32 v[14:15], v[138:139], s[16:17] op_sel_hi:[1,0]
	v_pk_mul_f32 v[6:7], v[10:11], v[6:7]
	v_pk_mul_f32 v[10:11], v[142:143], s[16:17] op_sel_hi:[1,0]
	v_rcp_f32_e32 v12, v12
	v_exp_f32_e32 v10, v10
	v_exp_f32_e32 v11, v11
	v_rcp_f32_e32 v13, v13
	v_exp_f32_e32 v14, v14
	v_exp_f32_e32 v15, v15
	v_pk_fma_f32 v[10:11], v[10:11], s[22:23], s[22:23] op_sel_hi:[1,0,0]
	v_pk_mul_f32 v[8:9], v[142:143], v[110:111]
	v_rcp_f32_e32 v10, v10
	v_rcp_f32_e32 v11, v11
	v_add_u32_e32 v5, 32, v4
	s_mov_b64 s[8:9], -1
	v_readlane_b32 s69, v254, 29
	v_pk_mul_f32 v[8:9], v[8:9], v[10:11]
	v_pk_mul_f32 v[10:11], v[136:137], v[104:105]
	v_readlane_b32 s70, v254, 30
	v_pk_mul_f32 v[10:11], v[10:11], v[12:13]
	v_pk_fma_f32 v[12:13], v[14:15], s[22:23], s[22:23] op_sel_hi:[1,0,0]
	v_mov_b32_e32 v15, 0
	v_rcp_f32_e32 v12, v12
	v_rcp_f32_e32 v13, v13
	v_cvt_pk_fp8_f32 v15, v10, v11
	v_mov_b32_e32 v14, 0
	v_cvt_pk_fp8_f32 v14, v6, v7
	v_pk_mul_f32 v[6:7], v[138:139], v[106:107]
	v_pk_mul_f32 v[10:11], v[132:133], v[100:101]
	v_pk_mul_f32 v[6:7], v[6:7], v[12:13]
	v_pk_mul_f32 v[12:13], v[128:129], s[16:17] op_sel_hi:[1,0]
	v_cvt_pk_fp8_f32 v15, v6, v7 op_sel:[0,0,1]
	v_pk_mul_f32 v[6:7], v[132:133], s[16:17] op_sel_hi:[1,0]
	v_cvt_pk_fp8_f32 v14, v8, v9 op_sel:[0,0,1]
	v_exp_f32_e32 v6, v6
	v_exp_f32_e32 v7, v7
	v_exp_f32_e32 v12, v12
	v_exp_f32_e32 v13, v13
	v_mad_i64_i32 v[8:9], s[44:45], v5, s58, v[2:3]
	v_pk_fma_f32 v[6:7], v[6:7], s[22:23], s[22:23] op_sel_hi:[1,0,0]
	v_lshl_add_u64 v[8:9], v[8:9], 0, v[0:1]
	v_rcp_f32_e32 v6, v6
	v_rcp_f32_e32 v7, v7
	global_store_dwordx2 v[8:9], v[14:15], off
	v_pk_fma_f32 v[12:13], v[12:13], s[22:23], s[22:23] op_sel_hi:[1,0,0]
	v_pk_mul_f32 v[14:15], v[130:131], s[16:17] op_sel_hi:[1,0]
	v_pk_mul_f32 v[6:7], v[10:11], v[6:7]
	v_pk_mul_f32 v[10:11], v[134:135], s[16:17] op_sel_hi:[1,0]
; __device__ __forceinline__ unsigned cvt_pk4_fp8(float a, float b, float c, float d) { int w = 0; w = __builtin_amdgcn_cvt_pk_fp8_f32(a, b, w, false); w = __builtin_amdgcn_cvt_pk_fp8_f32(c, d, w, true); return (unsigned)w; }
; __device__ __forceinline__ unsigned cvt_pk_bf16(float lo, float hi) { unsigned r; asm volatile("v_cvt_pk_bf16_f32 %0, %1, %2" : "=v"(r) : "v"(lo), "v"(hi)); return r; }
; __device__ __forceinline__ f32x2p silu_mul2k(f32x2p ag, f32x2p au, float kt, float ci) { const f32x2p t = ag * kt; f32x2p e; e.x = __builtin_amdgcn_exp2f(t.x); e.y = __builtin_amdgcn_exp2f(t.y);
;     const f32x2p d = e * ci + ci; f32x2p r; r.x = __builtin_amdgcn_rcpf(d.x); r.y = __builtin_amdgcn_rcpf(d.y); return (ag * au) * r; }
;     __device__ __forceinline__ void operator()(const f32x4 (&acc)[2][2][4][2], const Unit& u, int wr, int wc, int fr, int fq) const {
;         const int row0 = u.orow + wr * 64 + fr, col0 = u.ocol * HALF + wc * 32 + 8 * fq;
;         const float kt = -1.4426950408889634f * sc, ci = 1.f / (sc * sc * oscale);
; #pragma unroll
;         for (int ai = 0; ai < 2; ++ai)
; #pragma unroll
;             for (int m = 0; m < 4; ++m) { const size_t off = (size_t)(row0 + ai * HALF + m * 16) * ldc + col0;
;                 const f32x4 g0 = acc[ai][0][m][0], g1 = acc[ai][0][m][1], u0 = acc[ai][1][m][0], u1 = acc[ai][1][m][1];
;                 float v[8];
;                 { const f32x2p a = silu_mul2k((f32x2p){g0[0], g0[1]}, (f32x2p){u0[0], u0[1]}, kt, ci), b = silu_mul2k((f32x2p){g0[2], g0[3]}, (f32x2p){u0[2], u0[3]}, kt, ci), c = silu_mul2k((f32x2p){g1[0], g1[1]}, (f32x2p){u1[0], u1[1]}, kt, ci), d = silu_mul2k((f32x2p){g1[2], g1[3]}, (f32x2p){u1[2], u1[3]}, kt, ci);
;                   v[0] = a.x; v[1] = a.y; v[2] = b.x; v[3] = b.y; v[4] = c.x; v[5] = c.y; v[6] = d.x; v[7] = d.y; }
;                 if constexpr (FP8OUT) { typedef unsigned u32x2 __attribute__((ext_vector_type(2))); u32x2 w; w.x = cvt_pk4_fp8(v[0], v[1], v[2], v[3]); w.y = cvt_pk4_fp8(v[4], v[5], v[6], v[7]); __builtin_nontemporal_store(w, (u32x2*)((unsigned char*)O + off)); }
;                 else { u32x4 w; w.x = cvt_pk_bf16(v[0], v[1]); w.y = cvt_pk_bf16(v[2], v[3]); w.z = cvt_pk_bf16(v[4], v[5]); w.w = cvt_pk_bf16(v[6], v[7]); __builtin_nontemporal_store(w, (u32x4*)((bf16_t*)O + off)); } }
	v_rcp_f32_e32 v12, v12
	v_exp_f32_e32 v10, v10
	v_exp_f32_e32 v11, v11
	v_rcp_f32_e32 v13, v13
	v_exp_f32_e32 v14, v14
	v_exp_f32_e32 v15, v15
	v_pk_fma_f32 v[10:11], v[10:11], s[22:23], s[22:23] op_sel_hi:[1,0,0]
	v_pk_mul_f32 v[8:9], v[134:135], v[102:103]
	v_rcp_f32_e32 v10, v10
	v_rcp_f32_e32 v11, v11
	v_add_u32_e32 v5, 48, v4
	v_readlane_b32 s71, v254, 31
	v_readlane_b32 s72, v254, 32
	v_pk_mul_f32 v[8:9], v[8:9], v[10:11]
	v_pk_mul_f32 v[10:11], v[128:129], v[96:97]
	v_readlane_b32 s73, v254, 33
	v_pk_mul_f32 v[10:11], v[10:11], v[12:13]
	v_pk_fma_f32 v[12:13], v[14:15], s[22:23], s[22:23] op_sel_hi:[1,0,0]
	v_mov_b32_e32 v15, 0
	v_rcp_f32_e32 v12, v12
	v_rcp_f32_e32 v13, v13
	v_cvt_pk_fp8_f32 v15, v10, v11
	v_mov_b32_e32 v14, 0
	v_cvt_pk_fp8_f32 v14, v6, v7
	v_pk_mul_f32 v[6:7], v[130:131], v[98:99]
	v_pk_mul_f32 v[10:11], v[92:93], v[60:61]
	v_pk_mul_f32 v[6:7], v[6:7], v[12:13]
	v_pk_mul_f32 v[12:13], v[88:89], s[16:17] op_sel_hi:[1,0]
	v_cvt_pk_fp8_f32 v15, v6, v7 op_sel:[0,0,1]
	v_pk_mul_f32 v[6:7], v[92:93], s[16:17] op_sel_hi:[1,0]
	v_cvt_pk_fp8_f32 v14, v8, v9 op_sel:[0,0,1]
	v_exp_f32_e32 v6, v6
	v_exp_f32_e32 v7, v7
	v_exp_f32_e32 v12, v12
	v_exp_f32_e32 v13, v13
	v_mad_i64_i32 v[8:9], s[44:45], v5, s58, v[2:3]
	v_pk_fma_f32 v[6:7], v[6:7], s[22:23], s[22:23] op_sel_hi:[1,0,0]
	v_lshl_add_u64 v[8:9], v[8:9], 0, v[0:1]
	v_rcp_f32_e32 v6, v6
	v_rcp_f32_e32 v7, v7
	global_store_dwordx2 v[8:9], v[14:15], off
	v_pk_fma_f32 v[12:13], v[12:13], s[22:23], s[22:23] op_sel_hi:[1,0,0]
	v_pk_mul_f32 v[14:15], v[90:91], s[16:17] op_sel_hi:[1,0]
	v_pk_mul_f32 v[6:7], v[10:11], v[6:7]
	v_pk_mul_f32 v[10:11], v[94:95], s[16:17] op_sel_hi:[1,0]
	v_rcp_f32_e32 v12, v12
	v_exp_f32_e32 v10, v10
	v_exp_f32_e32 v11, v11
	v_rcp_f32_e32 v13, v13
	v_exp_f32_e32 v14, v14
	v_exp_f32_e32 v15, v15
	v_pk_fma_f32 v[10:11], v[10:11], s[22:23], s[22:23] op_sel_hi:[1,0,0]
	v_pk_mul_f32 v[8:9], v[94:95], v[62:63]
	v_rcp_f32_e32 v10, v10
	v_rcp_f32_e32 v11, v11
	v_add_u32_e32 v5, 0x80, v4
	v_readlane_b32 s74, v254, 34
	v_readlane_b32 s75, v254, 35
	v_pk_mul_f32 v[8:9], v[8:9], v[10:11]
	v_pk_mul_f32 v[10:11], v[88:89], v[56:57]
	s_nop 0
	v_pk_mul_f32 v[10:11], v[10:11], v[12:13]
	v_pk_fma_f32 v[12:13], v[14:15], s[22:23], s[22:23] op_sel_hi:[1,0,0]
	v_mov_b32_e32 v15, 0
	v_rcp_f32_e32 v12, v12
	v_rcp_f32_e32 v13, v13
	v_cvt_pk_fp8_f32 v15, v10, v11
	v_mov_b32_e32 v14, 0
	v_cvt_pk_fp8_f32 v14, v6, v7
	v_pk_mul_f32 v[6:7], v[90:91], v[58:59]
	v_pk_mul_f32 v[10:11], v[84:85], v[52:53]
	v_pk_mul_f32 v[6:7], v[6:7], v[12:13]
	v_pk_mul_f32 v[12:13], v[80:81], s[16:17] op_sel_hi:[1,0]
	v_cvt_pk_fp8_f32 v15, v6, v7 op_sel:[0,0,1]
	v_pk_mul_f32 v[6:7], v[84:85], s[16:17] op_sel_hi:[1,0]
	v_cvt_pk_fp8_f32 v14, v8, v9 op_sel:[0,0,1]
	v_exp_f32_e32 v6, v6
	v_exp_f32_e32 v7, v7
	v_exp_f32_e32 v12, v12
	v_exp_f32_e32 v13, v13
	v_mad_i64_i32 v[8:9], s[44:45], v5, s58, v[2:3]
	v_pk_fma_f32 v[6:7], v[6:7], s[22:23], s[22:23] op_sel_hi:[1,0,0]
	v_lshl_add_u64 v[8:9], v[8:9], 0, v[0:1]
	v_rcp_f32_e32 v6, v6
	v_rcp_f32_e32 v7, v7
	global_store_dwordx2 v[8:9], v[14:15], off
	v_pk_fma_f32 v[12:13], v[12:13], s[22:23], s[22:23] op_sel_hi:[1,0,0]
	v_pk_mul_f32 v[14:15], v[82:83], s[16:17] op_sel_hi:[1,0]
	v_pk_mul_f32 v[6:7], v[10:11], v[6:7]
	v_pk_mul_f32 v[10:11], v[86:87], s[16:17] op_sel_hi:[1,0]
	v_rcp_f32_e32 v12, v12
	v_exp_f32_e32 v10, v10
	v_exp_f32_e32 v11, v11
	v_rcp_f32_e32 v13, v13
	v_exp_f32_e32 v14, v14
	v_exp_f32_e32 v15, v15
	v_pk_fma_f32 v[10:11], v[10:11], s[22:23], s[22:23] op_sel_hi:[1,0,0]
	v_pk_mul_f32 v[8:9], v[86:87], v[54:55]
	v_rcp_f32_e32 v10, v10
	v_rcp_f32_e32 v11, v11
	v_add_u32_e32 v5, 0x90, v4
	v_pk_mul_f32 v[8:9], v[8:9], v[10:11]
	v_pk_mul_f32 v[10:11], v[80:81], v[48:49]
	s_nop 0
	v_pk_mul_f32 v[10:11], v[10:11], v[12:13]
; __device__ __forceinline__ unsigned cvt_pk4_fp8(float a, float b, float c, float d) { int w = 0; w = __builtin_amdgcn_cvt_pk_fp8_f32(a, b, w, false); w = __builtin_amdgcn_cvt_pk_fp8_f32(c, d, w, true); return (unsigned)w; }
; __device__ __forceinline__ unsigned cvt_pk_bf16(float lo, float hi) { unsigned r; asm volatile("v_cvt_pk_bf16_f32 %0, %1, %2" : "=v"(r) : "v"(lo), "v"(hi)); return r; }
; __device__ __forceinline__ f32x2p silu_mul2k(f32x2p ag, f32x2p au, float kt, float ci) { const f32x2p t = ag * kt; f32x2p e; e.x = __builtin_amdgcn_exp2f(t.x); e.y = __builtin_amdgcn_exp2f(t.y);
;     const f32x2p d = e * ci + ci; f32x2p r; r.x = __builtin_amdgcn_rcpf(d.x); r.y = __builtin_amdgcn_rcpf(d.y); return (ag * au) * r; }
;     __device__ __forceinline__ void operator()(const f32x4 (&acc)[2][2][4][2], const Unit& u, int wr, int wc, int fr, int fq) const {
;         const int row0 = u.orow + wr * 64 + fr, col0 = u.ocol * HALF + wc * 32 + 8 * fq;
;         const float kt = -1.4426950408889634f * sc, ci = 1.f / (sc * sc * oscale);
; #pragma unroll
;         for (int ai = 0; ai < 2; ++ai)
; #pragma unroll
;             for (int m = 0; m < 4; ++m) { const size_t off = (size_t)(row0 + ai * HALF + m * 16) * ldc + col0;
;                 const f32x4 g0 = acc[ai][0][m][0], g1 = acc[ai][0][m][1], u0 = acc[ai][1][m][0], u1 = acc[ai][1][m][1];
;                 float v[8];
;                 { const f32x2p a = silu_mul2k((f32x2p){g0[0], g0[1]}, (f32x2p){u0[0], u0[1]}, kt, ci), b = silu_mul2k((f32x2p){g0[2], g0[3]}, (f32x2p){u0[2], u0[3]}, kt, ci), c = silu_mul2k((f32x2p){g1[0], g1[1]}, (f32x2p){u1[0], u1[1]}, kt, ci), d = silu_mul2k((f32x2p){g1[2], g1[3]}, (f32x2p){u1[2], u1[3]}, kt, ci);
;                   v[0] = a.x; v[1] = a.y; v[2] = b.x; v[3] = b.y; v[4] = c.x; v[5] = c.y; v[6] = d.x; v[7] = d.y; }
;                 if constexpr (FP8OUT) { typedef unsigned u32x2 __attribute__((ext_vector_type(2))); u32x2 w; w.x = cvt_pk4_fp8(v[0], v[1], v[2], v[3]); w.y = cvt_pk4_fp8(v[4], v[5], v[6], v[7]); __builtin_nontemporal_store(w, (u32x2*)((unsigned char*)O + off)); }
;                 else { u32x4 w; w.x = cvt_pk_bf16(v[0], v[1]); w.y = cvt_pk_bf16(v[2], v[3]); w.z = cvt_pk_bf16(v[4], v[5]); w.w = cvt_pk_bf16(v[6], v[7]); __builtin_nontemporal_store(w, (u32x4*)((bf16_t*)O + off)); } }
	v_pk_fma_f32 v[12:13], v[14:15], s[22:23], s[22:23] op_sel_hi:[1,0,0]
	v_mov_b32_e32 v15, 0
	v_rcp_f32_e32 v12, v12
	v_rcp_f32_e32 v13, v13
	v_cvt_pk_fp8_f32 v15, v10, v11
	v_mov_b32_e32 v14, 0
	v_cvt_pk_fp8_f32 v14, v6, v7
	v_pk_mul_f32 v[6:7], v[82:83], v[50:51]
	v_pk_mul_f32 v[10:11], v[76:77], v[44:45]
	v_pk_mul_f32 v[6:7], v[6:7], v[12:13]
	v_pk_mul_f32 v[12:13], v[72:73], s[16:17] op_sel_hi:[1,0]
	v_cvt_pk_fp8_f32 v15, v6, v7 op_sel:[0,0,1]
	v_pk_mul_f32 v[6:7], v[76:77], s[16:17] op_sel_hi:[1,0]
	v_cvt_pk_fp8_f32 v14, v8, v9 op_sel:[0,0,1]
	v_exp_f32_e32 v6, v6
	v_exp_f32_e32 v7, v7
	v_exp_f32_e32 v12, v12
	v_exp_f32_e32 v13, v13
	v_mad_i64_i32 v[8:9], s[44:45], v5, s58, v[2:3]
	v_pk_fma_f32 v[6:7], v[6:7], s[22:23], s[22:23] op_sel_hi:[1,0,0]
	v_lshl_add_u64 v[8:9], v[8:9], 0, v[0:1]
	v_rcp_f32_e32 v6, v6
	v_rcp_f32_e32 v7, v7
	global_store_dwordx2 v[8:9], v[14:15], off
	v_pk_fma_f32 v[12:13], v[12:13], s[22:23], s[22:23] op_sel_hi:[1,0,0]
	v_pk_mul_f32 v[14:15], v[74:75], s[16:17] op_sel_hi:[1,0]
	v_pk_mul_f32 v[6:7], v[10:11], v[6:7]
	v_pk_mul_f32 v[10:11], v[78:79], s[16:17] op_sel_hi:[1,0]
	v_rcp_f32_e32 v12, v12
	v_exp_f32_e32 v10, v10
	v_exp_f32_e32 v11, v11
	v_rcp_f32_e32 v13, v13
	v_exp_f32_e32 v14, v14
	v_exp_f32_e32 v15, v15
	v_pk_fma_f32 v[10:11], v[10:11], s[22:23], s[22:23] op_sel_hi:[1,0,0]
	v_pk_mul_f32 v[8:9], v[78:79], v[46:47]
	v_rcp_f32_e32 v10, v10
	v_rcp_f32_e32 v11, v11
	v_add_u32_e32 v5, 0xa0, v4
	v_pk_mul_f32 v[8:9], v[8:9], v[10:11]
	v_pk_mul_f32 v[10:11], v[72:73], v[40:41]
	s_nop 0
	v_pk_mul_f32 v[10:11], v[10:11], v[12:13]
	v_pk_fma_f32 v[12:13], v[14:15], s[22:23], s[22:23] op_sel_hi:[1,0,0]
	v_mov_b32_e32 v15, 0
	v_rcp_f32_e32 v12, v12
	v_rcp_f32_e32 v13, v13
	v_cvt_pk_fp8_f32 v15, v10, v11
	v_mov_b32_e32 v14, 0
	v_cvt_pk_fp8_f32 v14, v6, v7
	v_pk_mul_f32 v[6:7], v[74:75], v[42:43]
	v_pk_mul_f32 v[10:11], v[64:65], s[16:17] op_sel_hi:[1,0]
	v_pk_mul_f32 v[6:7], v[6:7], v[12:13]
	v_cvt_pk_fp8_f32 v14, v8, v9 op_sel:[0,0,1]
	v_cvt_pk_fp8_f32 v15, v6, v7 op_sel:[0,0,1]
	v_pk_mul_f32 v[6:7], v[68:69], s[16:17] op_sel_hi:[1,0]
	v_mad_i64_i32 v[8:9], s[44:45], v5, s58, v[2:3]
	v_exp_f32_e32 v6, v6
	v_exp_f32_e32 v7, v7
	v_lshl_add_u64 v[8:9], v[8:9], 0, v[0:1]
	global_store_dwordx2 v[8:9], v[14:15], off
	v_pk_mul_f32 v[8:9], v[68:69], v[36:37]
	v_pk_fma_f32 v[6:7], v[6:7], s[22:23], s[22:23] op_sel_hi:[1,0,0]
	v_exp_f32_e32 v10, v10
	v_rcp_f32_e32 v6, v6
	v_rcp_f32_e32 v7, v7
	v_exp_f32_e32 v11, v11
	v_pk_mul_f32 v[12:13], v[66:67], s[16:17] op_sel_hi:[1,0]
	v_add_u32_e32 v14, 0xb0, v4
	v_pk_mul_f32 v[6:7], v[8:9], v[6:7]
	v_pk_mul_f32 v[8:9], v[70:71], s[16:17] op_sel_hi:[1,0]
	v_pk_fma_f32 v[10:11], v[10:11], s[22:23], s[22:23] op_sel_hi:[1,0,0]
	v_exp_f32_e32 v8, v8
	v_exp_f32_e32 v9, v9
	v_rcp_f32_e32 v10, v10
	v_rcp_f32_e32 v11, v11
	v_exp_f32_e32 v12, v12
	v_pk_fma_f32 v[8:9], v[8:9], s[22:23], s[22:23] op_sel_hi:[1,0,0]
	v_exp_f32_e32 v13, v13
	v_rcp_f32_e32 v8, v8
	v_rcp_f32_e32 v9, v9
	v_pk_mul_f32 v[4:5], v[70:71], v[38:39]
	v_mad_i64_i32 v[2:3], s[44:45], v14, s58, v[2:3]
	v_pk_mul_f32 v[4:5], v[4:5], v[8:9]
	v_pk_mul_f32 v[8:9], v[64:65], v[32:33]
	v_lshl_add_u64 v[0:1], v[2:3], 0, v[0:1]
	v_pk_mul_f32 v[8:9], v[8:9], v[10:11]
	v_pk_fma_f32 v[10:11], v[12:13], s[22:23], s[22:23] op_sel_hi:[1,0,0]
	v_mov_b32_e32 v12, 0
	v_rcp_f32_e32 v10, v10
	v_rcp_f32_e32 v11, v11
	v_mov_b32_e32 v13, 0
	v_cvt_pk_fp8_f32 v12, v6, v7
	v_cvt_pk_fp8_f32 v13, v8, v9
	v_pk_mul_f32 v[6:7], v[66:67], v[34:35]
	v_cvt_pk_fp8_f32 v12, v4, v5 op_sel:[0,0,1]
	v_pk_mul_f32 v[6:7], v[6:7], v[10:11]
	s_nop 0
	v_cvt_pk_fp8_f32 v13, v6, v7 op_sel:[0,0,1]
	global_store_dwordx2 v[0:1], v[12:13], off
	s_cbranch_vccnz .LBB0_863
	s_andn2_b64 vcc, exec, s[4:5]
	s_cbranch_vccnz .LBB0_862
	s_barrier
	s_branch .LBB0_862

; __device__ __forceinline__ unsigned cvt_pk4_fp8(float a, float b, float c, float d) { int w = 0; w = __builtin_amdgcn_cvt_pk_fp8_f32(a, b, w, false); w = __builtin_amdgcn_cvt_pk_fp8_f32(c, d, w, true); return (unsigned)w; }
; __device__ __forceinline__ unsigned cvt_pk_bf16(float lo, float hi) { unsigned r; asm volatile("v_cvt_pk_bf16_f32 %0, %1, %2" : "=v"(r) : "v"(lo), "v"(hi)); return r; }
; __device__ __forceinline__ f32x2p silu_mul2k(f32x2p ag, f32x2p au, float kt, float ci) { const f32x2p t = ag * kt; f32x2p e; e.x = __builtin_amdgcn_exp2f(t.x); e.y = __builtin_amdgcn_exp2f(t.y);
;     const f32x2p d = e * ci + ci; f32x2p r; r.x = __builtin_amdgcn_rcpf(d.x); r.y = __builtin_amdgcn_rcpf(d.y); return (ag * au) * r; }
;     __device__ __forceinline__ void operator()(const f32x4 (&acc)[2][2][4][2], const Unit& u, int wr, int wc, int fr, int fq) const {
;         const int row0 = u.orow + wr * 64 + fr, col0 = u.ocol * HALF + wc * 32 + 8 * fq;
;         const float kt = -1.4426950408889634f * sc, ci = 1.f / (sc * sc * oscale);
; #pragma unroll
;         for (int ai = 0; ai < 2; ++ai)
; #pragma unroll
;             for (int m = 0; m < 4; ++m) { const size_t off = (size_t)(row0 + ai * HALF + m * 16) * ldc + col0;
;                 const f32x4 g0 = acc[ai][0][m][0], g1 = acc[ai][0][m][1], u0 = acc[ai][1][m][0], u1 = acc[ai][1][m][1];
;                 float v[8];
;                 { const f32x2p a = silu_mul2k((f32x2p){g0[0], g0[1]}, (f32x2p){u0[0], u0[1]}, kt, ci), b = silu_mul2k((f32x2p){g0[2], g0[3]}, (f32x2p){u0[2], u0[3]}, kt, ci), c = silu_mul2k((f32x2p){g1[0], g1[1]}, (f32x2p){u1[0], u1[1]}, kt, ci), d = silu_mul2k((f32x2p){g1[2], g1[3]}, (f32x2p){u1[2], u1[3]}, kt, ci);
;                   v[0] = a.x; v[1] = a.y; v[2] = b.x; v[3] = b.y; v[4] = c.x; v[5] = c.y; v[6] = d.x; v[7] = d.y; }
;                 if constexpr (FP8OUT) { typedef unsigned u32x2 __attribute__((ext_vector_type(2))); u32x2 w; w.x = cvt_pk4_fp8(v[0], v[1], v[2], v[3]); w.y = cvt_pk4_fp8(v[4], v[5], v[6], v[7]); __builtin_nontemporal_store(w, (u32x2*)((unsigned char*)O + off)); }
;                 else { u32x4 w; w.x = cvt_pk_bf16(v[0], v[1]); w.y = cvt_pk_bf16(v[2], v[3]); w.z = cvt_pk_bf16(v[4], v[5]); w.w = cvt_pk_bf16(v[6], v[7]); __builtin_nontemporal_store(w, (u32x4*)((bf16_t*)O + off)); } }
.LBB0_1764:
	v_pk_mul_f32 v[0:1], v[156:157], s[16:17] op_sel_hi:[1,0]
	v_pk_mul_f32 v[8:9], v[156:157], v[124:125]
	v_exp_f32_e32 v2, v0
	v_exp_f32_e32 v3, v1
	v_pk_mul_f32 v[10:11], v[152:153], s[16:17] op_sel_hi:[1,0]
	v_pk_mul_f32 v[12:13], v[154:155], s[16:17] op_sel_hi:[1,0]
	v_exp_f32_e32 v10, v10
	v_pk_fma_f32 v[2:3], v[2:3], s[22:23], s[22:23] op_sel_hi:[1,0,0]
	v_exp_f32_e32 v11, v11
	v_rcp_f32_e32 v2, v2
	v_rcp_f32_e32 v3, v3
	v_exp_f32_e32 v12, v12
	v_pk_fma_f32 v[10:11], v[10:11], s[22:23], s[22:23] op_sel_hi:[1,0,0]
	v_exp_f32_e32 v13, v13
	v_pk_mul_f32 v[2:3], v[8:9], v[2:3]
	v_pk_mul_f32 v[8:9], v[158:159], s[16:17] op_sel_hi:[1,0]
	v_rcp_f32_e32 v10, v10
	v_exp_f32_e32 v8, v8
	v_exp_f32_e32 v9, v9
	v_rcp_f32_e32 v11, v11
	v_pk_mul_f32 v[6:7], v[158:159], v[126:127]
	v_add_u32_e32 v4, s74, v182
	v_pk_fma_f32 v[8:9], v[8:9], s[22:23], s[22:23] op_sel_hi:[1,0,0]
	v_lshl_add_u32 v0, s67, 7, v184
	v_rcp_f32_e32 v8, v8
	v_rcp_f32_e32 v9, v9
	v_ashrrev_i32_e32 v1, 31, v0
	s_nop 15
	s_nop 15
	v_pk_mul_f32 v[14:15], v[146:147], s[16:17] op_sel_hi:[1,0]
	v_pk_mul_f32 v[6:7], v[6:7], v[8:9]
	v_pk_mul_f32 v[8:9], v[152:153], v[120:121]
	v_exp_f32_e32 v14, v14
	v_pk_mul_f32 v[8:9], v[8:9], v[10:11]
	v_pk_fma_f32 v[10:11], v[12:13], s[22:23], s[22:23] op_sel_hi:[1,0,0]
	v_mov_b32_e32 v12, 0
	v_cvt_pk_fp8_f32 v12, v2, v3
	v_rcp_f32_e32 v10, v10
	v_rcp_f32_e32 v11, v11
	v_mov_b32_e32 v13, 0
	v_cvt_pk_fp8_f32 v12, v6, v7 op_sel:[0,0,1]
	v_pk_mul_f32 v[6:7], v[148:149], s[16:17] op_sel_hi:[1,0]
	v_cvt_pk_fp8_f32 v13, v8, v9
	v_exp_f32_e32 v6, v6
	v_exp_f32_e32 v7, v7
	v_pk_mul_f32 v[2:3], v[154:155], v[122:123]
	v_exp_f32_e32 v15, v15
	v_pk_mul_f32 v[2:3], v[2:3], v[10:11]
	v_pk_fma_f32 v[6:7], v[6:7], s[22:23], s[22:23] op_sel_hi:[1,0,0]
	v_cvt_pk_fp8_f32 v13, v2, v3 op_sel:[0,0,1]
	v_rcp_f32_e32 v6, v6
	v_rcp_f32_e32 v7, v7
	v_mov_b64_e32 v[2:3], s[20:21]
	v_mad_i64_i32 v[8:9], s[38:39], v4, s64, v[2:3]
	v_pk_mul_f32 v[10:11], v[148:149], v[116:117]
	v_lshl_add_u64 v[8:9], v[8:9], 0, v[0:1]
	v_pk_mul_f32 v[6:7], v[10:11], v[6:7]
	v_pk_mul_f32 v[10:11], v[150:151], s[16:17] op_sel_hi:[1,0]
	global_store_dwordx2 v[8:9], v[12:13], off
	v_exp_f32_e32 v10, v10
	v_exp_f32_e32 v11, v11
	v_pk_mul_f32 v[12:13], v[144:145], s[16:17] op_sel_hi:[1,0]
	v_pk_mul_f32 v[8:9], v[150:151], v[118:119]
	v_exp_f32_e32 v12, v12
	v_exp_f32_e32 v13, v13
	v_pk_fma_f32 v[10:11], v[10:11], s[22:23], s[22:23] op_sel_hi:[1,0,0]
	v_add_u32_e32 v5, 16, v4
	v_rcp_f32_e32 v10, v10
	v_rcp_f32_e32 v11, v11
	v_pk_fma_f32 v[12:13], v[12:13], s[22:23], s[22:23] op_sel_hi:[1,0,0]
	s_andn2_b64 vcc, exec, s[4:5]
	v_rcp_f32_e32 v12, v12
	v_rcp_f32_e32 v13, v13
	v_pk_mul_f32 v[8:9], v[8:9], v[10:11]
	v_pk_mul_f32 v[10:11], v[144:145], v[112:113]
	s_mov_b64 s[4:5], -1
	v_pk_mul_f32 v[10:11], v[10:11], v[12:13]
	v_pk_fma_f32 v[12:13], v[14:15], s[22:23], s[22:23] op_sel_hi:[1,0,0]
	v_mov_b32_e32 v15, 0
	v_rcp_f32_e32 v12, v12
	v_rcp_f32_e32 v13, v13
	v_cvt_pk_fp8_f32 v15, v10, v11
	v_mov_b32_e32 v14, 0
	v_cvt_pk_fp8_f32 v14, v6, v7
	v_pk_mul_f32 v[6:7], v[146:147], v[114:115]
	v_pk_mul_f32 v[10:11], v[140:141], v[108:109]
	v_pk_mul_f32 v[6:7], v[6:7], v[12:13]
	v_pk_mul_f32 v[12:13], v[136:137], s[16:17] op_sel_hi:[1,0]
	v_cvt_pk_fp8_f32 v15, v6, v7 op_sel:[0,0,1]
	v_pk_mul_f32 v[6:7], v[140:141], s[16:17] op_sel_hi:[1,0]
	v_cvt_pk_fp8_f32 v14, v8, v9 op_sel:[0,0,1]
	v_exp_f32_e32 v6, v6
	v_exp_f32_e32 v7, v7
	v_exp_f32_e32 v12, v12
	v_exp_f32_e32 v13, v13
	v_mad_i64_i32 v[8:9], s[38:39], v5, s64, v[2:3]
	v_pk_fma_f32 v[6:7], v[6:7], s[22:23], s[22:23] op_sel_hi:[1,0,0]
	v_lshl_add_u64 v[8:9], v[8:9], 0, v[0:1]
	v_rcp_f32_e32 v6, v6
	v_rcp_f32_e32 v7, v7
	global_store_dwordx2 v[8:9], v[14:15], off
	v_pk_fma_f32 v[12:13], v[12:13], s[22:23], s[22:23] op_sel_hi:[1,0,0]
	v_pk_mul_f32 v[14:15], v[138:139], s[16:17] op_sel_hi:[1,0]
	v_pk_mul_f32 v[6:7], v[10:11], v[6:7]
	v_pk_mul_f32 v[10:11], v[142:143], s[16:17] op_sel_hi:[1,0]
	v_rcp_f32_e32 v12, v12
	v_exp_f32_e32 v10, v10
	v_exp_f32_e32 v11, v11
	v_rcp_f32_e32 v13, v13
	v_exp_f32_e32 v14, v14
	v_exp_f32_e32 v15, v15
	v_pk_fma_f32 v[10:11], v[10:11], s[22:23], s[22:23] op_sel_hi:[1,0,0]
	v_pk_mul_f32 v[8:9], v[142:143], v[110:111]
	v_rcp_f32_e32 v10, v10
	v_rcp_f32_e32 v11, v11
	v_add_u32_e32 v5, 32, v4
	v_pk_mul_f32 v[8:9], v[8:9], v[10:11]
	v_pk_mul_f32 v[10:11], v[136:137], v[104:105]
	s_nop 0
	v_pk_mul_f32 v[10:11], v[10:11], v[12:13]
	v_pk_fma_f32 v[12:13], v[14:15], s[22:23], s[22:23] op_sel_hi:[1,0,0]
	v_mov_b32_e32 v15, 0
	v_rcp_f32_e32 v12, v12
	v_rcp_f32_e32 v13, v13
	v_cvt_pk_fp8_f32 v15, v10, v11
	v_mov_b32_e32 v14, 0
	v_cvt_pk_fp8_f32 v14, v6, v7
	v_pk_mul_f32 v[6:7], v[138:139], v[106:107]
	v_pk_mul_f32 v[10:11], v[132:133], v[100:101]
	v_pk_mul_f32 v[6:7], v[6:7], v[12:13]
	v_pk_mul_f32 v[12:13], v[128:129], s[16:17] op_sel_hi:[1,0]
	v_cvt_pk_fp8_f32 v15, v6, v7 op_sel:[0,0,1]
	v_pk_mul_f32 v[6:7], v[132:133], s[16:17] op_sel_hi:[1,0]
	v_cvt_pk_fp8_f32 v14, v8, v9 op_sel:[0,0,1]
	v_exp_f32_e32 v6, v6
	v_exp_f32_e32 v7, v7
	v_exp_f32_e32 v12, v12
	v_exp_f32_e32 v13, v13
	v_mad_i64_i32 v[8:9], s[38:39], v5, s64, v[2:3]
	v_pk_fma_f32 v[6:7], v[6:7], s[22:23], s[22:23] op_sel_hi:[1,0,0]
	v_lshl_add_u64 v[8:9], v[8:9], 0, v[0:1]
	v_rcp_f32_e32 v6, v6
	v_rcp_f32_e32 v7, v7
	global_store_dwordx2 v[8:9], v[14:15], off
	v_pk_fma_f32 v[12:13], v[12:13], s[22:23], s[22:23] op_sel_hi:[1,0,0]
	v_pk_mul_f32 v[14:15], v[130:131], s[16:17] op_sel_hi:[1,0]
	v_pk_mul_f32 v[6:7], v[10:11], v[6:7]
	v_pk_mul_f32 v[10:11], v[134:135], s[16:17] op_sel_hi:[1,0]
	v_rcp_f32_e32 v12, v12
	v_exp_f32_e32 v10, v10
	v_exp_f32_e32 v11, v11
; __device__ __forceinline__ unsigned cvt_pk4_fp8(float a, float b, float c, float d) { int w = 0; w = __builtin_amdgcn_cvt_pk_fp8_f32(a, b, w, false); w = __builtin_amdgcn_cvt_pk_fp8_f32(c, d, w, true); return (unsigned)w; }
; __device__ __forceinline__ unsigned cvt_pk_bf16(float lo, float hi) { unsigned r; asm volatile("v_cvt_pk_bf16_f32 %0, %1, %2" : "=v"(r) : "v"(lo), "v"(hi)); return r; }
; __device__ __forceinline__ f32x2p silu_mul2k(f32x2p ag, f32x2p au, float kt, float ci) { const f32x2p t = ag * kt; f32x2p e; e.x = __builtin_amdgcn_exp2f(t.x); e.y = __builtin_amdgcn_exp2f(t.y);
;     const f32x2p d = e * ci + ci; f32x2p r; r.x = __builtin_amdgcn_rcpf(d.x); r.y = __builtin_amdgcn_rcpf(d.y); return (ag * au) * r; }
;     __device__ __forceinline__ void operator()(const f32x4 (&acc)[2][2][4][2], const Unit& u, int wr, int wc, int fr, int fq) const {
;         const int row0 = u.orow + wr * 64 + fr, col0 = u.ocol * HALF + wc * 32 + 8 * fq;
;         const float kt = -1.4426950408889634f * sc, ci = 1.f / (sc * sc * oscale);
; #pragma unroll
;         for (int ai = 0; ai < 2; ++ai)
; #pragma unroll
;             for (int m = 0; m < 4; ++m) { const size_t off = (size_t)(row0 + ai * HALF + m * 16) * ldc + col0;
;                 const f32x4 g0 = acc[ai][0][m][0], g1 = acc[ai][0][m][1], u0 = acc[ai][1][m][0], u1 = acc[ai][1][m][1];
;                 float v[8];
;                 { const f32x2p a = silu_mul2k((f32x2p){g0[0], g0[1]}, (f32x2p){u0[0], u0[1]}, kt, ci), b = silu_mul2k((f32x2p){g0[2], g0[3]}, (f32x2p){u0[2], u0[3]}, kt, ci), c = silu_mul2k((f32x2p){g1[0], g1[1]}, (f32x2p){u1[0], u1[1]}, kt, ci), d = silu_mul2k((f32x2p){g1[2], g1[3]}, (f32x2p){u1[2], u1[3]}, kt, ci);
;                   v[0] = a.x; v[1] = a.y; v[2] = b.x; v[3] = b.y; v[4] = c.x; v[5] = c.y; v[6] = d.x; v[7] = d.y; }
;                 if constexpr (FP8OUT) { typedef unsigned u32x2 __attribute__((ext_vector_type(2))); u32x2 w; w.x = cvt_pk4_fp8(v[0], v[1], v[2], v[3]); w.y = cvt_pk4_fp8(v[4], v[5], v[6], v[7]); __builtin_nontemporal_store(w, (u32x2*)((unsigned char*)O + off)); }
;                 else { u32x4 w; w.x = cvt_pk_bf16(v[0], v[1]); w.y = cvt_pk_bf16(v[2], v[3]); w.z = cvt_pk_bf16(v[4], v[5]); w.w = cvt_pk_bf16(v[6], v[7]); __builtin_nontemporal_store(w, (u32x4*)((bf16_t*)O + off)); } }
	v_rcp_f32_e32 v13, v13
	v_exp_f32_e32 v14, v14
	v_exp_f32_e32 v15, v15
	v_pk_fma_f32 v[10:11], v[10:11], s[22:23], s[22:23] op_sel_hi:[1,0,0]
	v_pk_mul_f32 v[8:9], v[134:135], v[102:103]
	v_rcp_f32_e32 v10, v10
	v_rcp_f32_e32 v11, v11
	v_add_u32_e32 v5, 48, v4
	v_pk_mul_f32 v[8:9], v[8:9], v[10:11]
	v_pk_mul_f32 v[10:11], v[128:129], v[96:97]
	s_nop 0
	v_pk_mul_f32 v[10:11], v[10:11], v[12:13]
	v_pk_fma_f32 v[12:13], v[14:15], s[22:23], s[22:23] op_sel_hi:[1,0,0]
	v_mov_b32_e32 v15, 0
	v_rcp_f32_e32 v12, v12
	v_rcp_f32_e32 v13, v13
	v_cvt_pk_fp8_f32 v15, v10, v11
	v_mov_b32_e32 v14, 0
	v_cvt_pk_fp8_f32 v14, v6, v7
	v_pk_mul_f32 v[6:7], v[130:131], v[98:99]
	v_pk_mul_f32 v[10:11], v[92:93], v[60:61]
	v_pk_mul_f32 v[6:7], v[6:7], v[12:13]
	v_pk_mul_f32 v[12:13], v[88:89], s[16:17] op_sel_hi:[1,0]
	v_cvt_pk_fp8_f32 v15, v6, v7 op_sel:[0,0,1]
	v_pk_mul_f32 v[6:7], v[92:93], s[16:17] op_sel_hi:[1,0]
	v_cvt_pk_fp8_f32 v14, v8, v9 op_sel:[0,0,1]
	v_exp_f32_e32 v6, v6
	v_exp_f32_e32 v7, v7
	v_exp_f32_e32 v12, v12
	v_exp_f32_e32 v13, v13
	v_mad_i64_i32 v[8:9], s[38:39], v5, s64, v[2:3]
	v_pk_fma_f32 v[6:7], v[6:7], s[22:23], s[22:23] op_sel_hi:[1,0,0]
	v_lshl_add_u64 v[8:9], v[8:9], 0, v[0:1]
	v_rcp_f32_e32 v6, v6
	v_rcp_f32_e32 v7, v7
	global_store_dwordx2 v[8:9], v[14:15], off
	v_pk_fma_f32 v[12:13], v[12:13], s[22:23], s[22:23] op_sel_hi:[1,0,0]
	v_pk_mul_f32 v[14:15], v[90:91], s[16:17] op_sel_hi:[1,0]
	v_pk_mul_f32 v[6:7], v[10:11], v[6:7]
	v_pk_mul_f32 v[10:11], v[94:95], s[16:17] op_sel_hi:[1,0]
	v_rcp_f32_e32 v12, v12
	v_exp_f32_e32 v10, v10
	v_exp_f32_e32 v11, v11
	v_rcp_f32_e32 v13, v13
	v_exp_f32_e32 v14, v14
	v_exp_f32_e32 v15, v15
	v_pk_fma_f32 v[10:11], v[10:11], s[22:23], s[22:23] op_sel_hi:[1,0,0]
	v_pk_mul_f32 v[8:9], v[94:95], v[62:63]
	v_rcp_f32_e32 v10, v10
	v_rcp_f32_e32 v11, v11
	v_add_u32_e32 v5, 0x80, v4
	v_pk_mul_f32 v[8:9], v[8:9], v[10:11]
	v_pk_mul_f32 v[10:11], v[88:89], v[56:57]
	s_nop 0
	v_pk_mul_f32 v[10:11], v[10:11], v[12:13]
	v_pk_fma_f32 v[12:13], v[14:15], s[22:23], s[22:23] op_sel_hi:[1,0,0]
	v_mov_b32_e32 v15, 0
	v_rcp_f32_e32 v12, v12
	v_rcp_f32_e32 v13, v13
	v_cvt_pk_fp8_f32 v15, v10, v11
	v_mov_b32_e32 v14, 0
	v_cvt_pk_fp8_f32 v14, v6, v7
	v_pk_mul_f32 v[6:7], v[90:91], v[58:59]
	v_pk_mul_f32 v[10:11], v[84:85], v[52:53]
	v_pk_mul_f32 v[6:7], v[6:7], v[12:13]
	v_pk_mul_f32 v[12:13], v[80:81], s[16:17] op_sel_hi:[1,0]
	v_cvt_pk_fp8_f32 v15, v6, v7 op_sel:[0,0,1]
	v_pk_mul_f32 v[6:7], v[84:85], s[16:17] op_sel_hi:[1,0]
	v_cvt_pk_fp8_f32 v14, v8, v9 op_sel:[0,0,1]
	v_exp_f32_e32 v6, v6
	v_exp_f32_e32 v7, v7
	v_exp_f32_e32 v12, v12
	v_exp_f32_e32 v13, v13
	v_mad_i64_i32 v[8:9], s[38:39], v5, s64, v[2:3]
	v_pk_fma_f32 v[6:7], v[6:7], s[22:23], s[22:23] op_sel_hi:[1,0,0]
	v_lshl_add_u64 v[8:9], v[8:9], 0, v[0:1]
	v_rcp_f32_e32 v6, v6
	v_rcp_f32_e32 v7, v7
	global_store_dwordx2 v[8:9], v[14:15], off
	v_pk_fma_f32 v[12:13], v[12:13], s[22:23], s[22:23] op_sel_hi:[1,0,0]
	v_pk_mul_f32 v[14:15], v[82:83], s[16:17] op_sel_hi:[1,0]
	v_pk_mul_f32 v[6:7], v[10:11], v[6:7]
	v_pk_mul_f32 v[10:11], v[86:87], s[16:17] op_sel_hi:[1,0]
	v_rcp_f32_e32 v12, v12
	v_exp_f32_e32 v10, v10
	v_exp_f32_e32 v11, v11
	v_rcp_f32_e32 v13, v13
	v_exp_f32_e32 v14, v14
	v_exp_f32_e32 v15, v15
	v_pk_fma_f32 v[10:11], v[10:11], s[22:23], s[22:23] op_sel_hi:[1,0,0]
	v_pk_mul_f32 v[8:9], v[86:87], v[54:55]
	v_rcp_f32_e32 v10, v10
	v_rcp_f32_e32 v11, v11
	v_add_u32_e32 v5, 0x90, v4
	v_pk_mul_f32 v[8:9], v[8:9], v[10:11]
	v_pk_mul_f32 v[10:11], v[80:81], v[48:49]
	s_nop 0
	v_pk_mul_f32 v[10:11], v[10:11], v[12:13]
	v_pk_fma_f32 v[12:13], v[14:15], s[22:23], s[22:23] op_sel_hi:[1,0,0]
	v_mov_b32_e32 v15, 0
	v_rcp_f32_e32 v12, v12
; __device__ __forceinline__ unsigned cvt_pk4_fp8(float a, float b, float c, float d) { int w = 0; w = __builtin_amdgcn_cvt_pk_fp8_f32(a, b, w, false); w = __builtin_amdgcn_cvt_pk_fp8_f32(c, d, w, true); return (unsigned)w; }
; __device__ __forceinline__ unsigned cvt_pk_bf16(float lo, float hi) { unsigned r; asm volatile("v_cvt_pk_bf16_f32 %0, %1, %2" : "=v"(r) : "v"(lo), "v"(hi)); return r; }
; __device__ __forceinline__ f32x2p silu_mul2k(f32x2p ag, f32x2p au, float kt, float ci) { const f32x2p t = ag * kt; f32x2p e; e.x = __builtin_amdgcn_exp2f(t.x); e.y = __builtin_amdgcn_exp2f(t.y);
;     const f32x2p d = e * ci + ci; f32x2p r; r.x = __builtin_amdgcn_rcpf(d.x); r.y = __builtin_amdgcn_rcpf(d.y); return (ag * au) * r; }
;     __device__ __forceinline__ void operator()(const f32x4 (&acc)[2][2][4][2], const Unit& u, int wr, int wc, int fr, int fq) const {
;         const int row0 = u.orow + wr * 64 + fr, col0 = u.ocol * HALF + wc * 32 + 8 * fq;
;         const float kt = -1.4426950408889634f * sc, ci = 1.f / (sc * sc * oscale);
; #pragma unroll
;         for (int ai = 0; ai < 2; ++ai)
; #pragma unroll
;             for (int m = 0; m < 4; ++m) { const size_t off = (size_t)(row0 + ai * HALF + m * 16) * ldc + col0;
;                 const f32x4 g0 = acc[ai][0][m][0], g1 = acc[ai][0][m][1], u0 = acc[ai][1][m][0], u1 = acc[ai][1][m][1];
;                 float v[8];
;                 { const f32x2p a = silu_mul2k((f32x2p){g0[0], g0[1]}, (f32x2p){u0[0], u0[1]}, kt, ci), b = silu_mul2k((f32x2p){g0[2], g0[3]}, (f32x2p){u0[2], u0[3]}, kt, ci), c = silu_mul2k((f32x2p){g1[0], g1[1]}, (f32x2p){u1[0], u1[1]}, kt, ci), d = silu_mul2k((f32x2p){g1[2], g1[3]}, (f32x2p){u1[2], u1[3]}, kt, ci);
;                   v[0] = a.x; v[1] = a.y; v[2] = b.x; v[3] = b.y; v[4] = c.x; v[5] = c.y; v[6] = d.x; v[7] = d.y; }
;                 if constexpr (FP8OUT) { typedef unsigned u32x2 __attribute__((ext_vector_type(2))); u32x2 w; w.x = cvt_pk4_fp8(v[0], v[1], v[2], v[3]); w.y = cvt_pk4_fp8(v[4], v[5], v[6], v[7]); __builtin_nontemporal_store(w, (u32x2*)((unsigned char*)O + off)); }
;                 else { u32x4 w; w.x = cvt_pk_bf16(v[0], v[1]); w.y = cvt_pk_bf16(v[2], v[3]); w.z = cvt_pk_bf16(v[4], v[5]); w.w = cvt_pk_bf16(v[6], v[7]); __builtin_nontemporal_store(w, (u32x4*)((bf16_t*)O + off)); } }
	v_rcp_f32_e32 v13, v13
	v_cvt_pk_fp8_f32 v15, v10, v11
	v_mov_b32_e32 v14, 0
	v_cvt_pk_fp8_f32 v14, v6, v7
	v_pk_mul_f32 v[6:7], v[82:83], v[50:51]
	v_pk_mul_f32 v[10:11], v[76:77], v[44:45]
	v_pk_mul_f32 v[6:7], v[6:7], v[12:13]
	v_pk_mul_f32 v[12:13], v[72:73], s[16:17] op_sel_hi:[1,0]
	v_cvt_pk_fp8_f32 v15, v6, v7 op_sel:[0,0,1]
	v_pk_mul_f32 v[6:7], v[76:77], s[16:17] op_sel_hi:[1,0]
	v_cvt_pk_fp8_f32 v14, v8, v9 op_sel:[0,0,1]
	v_exp_f32_e32 v6, v6
	v_exp_f32_e32 v7, v7
	v_exp_f32_e32 v12, v12
	v_exp_f32_e32 v13, v13
	v_mad_i64_i32 v[8:9], s[38:39], v5, s64, v[2:3]
	v_pk_fma_f32 v[6:7], v[6:7], s[22:23], s[22:23] op_sel_hi:[1,0,0]
	v_lshl_add_u64 v[8:9], v[8:9], 0, v[0:1]
	v_rcp_f32_e32 v6, v6
	v_rcp_f32_e32 v7, v7
	global_store_dwordx2 v[8:9], v[14:15], off
	v_pk_fma_f32 v[12:13], v[12:13], s[22:23], s[22:23] op_sel_hi:[1,0,0]
	v_pk_mul_f32 v[14:15], v[74:75], s[16:17] op_sel_hi:[1,0]
	v_pk_mul_f32 v[6:7], v[10:11], v[6:7]
	v_pk_mul_f32 v[10:11], v[78:79], s[16:17] op_sel_hi:[1,0]
	v_rcp_f32_e32 v12, v12
	v_exp_f32_e32 v10, v10
	v_exp_f32_e32 v11, v11
	v_rcp_f32_e32 v13, v13
	v_exp_f32_e32 v14, v14
	v_exp_f32_e32 v15, v15
	v_pk_fma_f32 v[10:11], v[10:11], s[22:23], s[22:23] op_sel_hi:[1,0,0]
	v_pk_mul_f32 v[8:9], v[78:79], v[46:47]
	v_rcp_f32_e32 v10, v10
	v_rcp_f32_e32 v11, v11
	v_add_u32_e32 v5, 0xa0, v4
	v_pk_mul_f32 v[8:9], v[8:9], v[10:11]
	v_pk_mul_f32 v[10:11], v[72:73], v[40:41]
	s_nop 0
	v_pk_mul_f32 v[10:11], v[10:11], v[12:13]
	v_pk_fma_f32 v[12:13], v[14:15], s[22:23], s[22:23] op_sel_hi:[1,0,0]
	v_mov_b32_e32 v15, 0
	v_rcp_f32_e32 v12, v12
	v_rcp_f32_e32 v13, v13
	v_cvt_pk_fp8_f32 v15, v10, v11
	v_mov_b32_e32 v14, 0
	v_cvt_pk_fp8_f32 v14, v6, v7
	v_pk_mul_f32 v[6:7], v[74:75], v[42:43]
	v_pk_mul_f32 v[10:11], v[64:65], s[16:17] op_sel_hi:[1,0]
	v_pk_mul_f32 v[6:7], v[6:7], v[12:13]
	v_cvt_pk_fp8_f32 v14, v8, v9 op_sel:[0,0,1]
	v_cvt_pk_fp8_f32 v15, v6, v7 op_sel:[0,0,1]
	v_pk_mul_f32 v[6:7], v[68:69], s[16:17] op_sel_hi:[1,0]
	v_mad_i64_i32 v[8:9], s[38:39], v5, s64, v[2:3]
	v_exp_f32_e32 v6, v6
	v_exp_f32_e32 v7, v7
	v_lshl_add_u64 v[8:9], v[8:9], 0, v[0:1]
	global_store_dwordx2 v[8:9], v[14:15], off
	v_pk_mul_f32 v[8:9], v[68:69], v[36:37]
	v_pk_fma_f32 v[6:7], v[6:7], s[22:23], s[22:23] op_sel_hi:[1,0,0]
	v_exp_f32_e32 v10, v10
	v_rcp_f32_e32 v6, v6
	v_rcp_f32_e32 v7, v7
	v_exp_f32_e32 v11, v11
	v_pk_mul_f32 v[12:13], v[66:67], s[16:17] op_sel_hi:[1,0]
	v_add_u32_e32 v14, 0xb0, v4
	v_pk_mul_f32 v[6:7], v[8:9], v[6:7]
	v_pk_mul_f32 v[8:9], v[70:71], s[16:17] op_sel_hi:[1,0]
	v_pk_fma_f32 v[10:11], v[10:11], s[22:23], s[22:23] op_sel_hi:[1,0,0]
	v_exp_f32_e32 v8, v8
	v_exp_f32_e32 v9, v9
	v_rcp_f32_e32 v10, v10
	v_rcp_f32_e32 v11, v11
	v_exp_f32_e32 v12, v12
	v_pk_fma_f32 v[8:9], v[8:9], s[22:23], s[22:23] op_sel_hi:[1,0,0]
	v_exp_f32_e32 v13, v13
	v_rcp_f32_e32 v8, v8
	v_rcp_f32_e32 v9, v9
	v_pk_mul_f32 v[4:5], v[70:71], v[38:39]
	v_mad_i64_i32 v[2:3], s[38:39], v14, s64, v[2:3]
	v_pk_mul_f32 v[4:5], v[4:5], v[8:9]
	v_pk_mul_f32 v[8:9], v[64:65], v[32:33]
	v_lshl_add_u64 v[0:1], v[2:3], 0, v[0:1]
	v_pk_mul_f32 v[8:9], v[8:9], v[10:11]
	v_pk_fma_f32 v[10:11], v[12:13], s[22:23], s[22:23] op_sel_hi:[1,0,0]
	v_mov_b32_e32 v12, 0
	v_rcp_f32_e32 v10, v10
	v_rcp_f32_e32 v11, v11
	v_mov_b32_e32 v13, 0
	v_cvt_pk_fp8_f32 v12, v6, v7
	v_cvt_pk_fp8_f32 v13, v8, v9
	v_pk_mul_f32 v[6:7], v[66:67], v[34:35]
	v_cvt_pk_fp8_f32 v12, v4, v5 op_sel:[0,0,1]
	v_pk_mul_f32 v[6:7], v[6:7], v[10:11]
	s_nop 0
	v_cvt_pk_fp8_f32 v13, v6, v7 op_sel:[0,0,1]
	global_store_dwordx2 v[0:1], v[12:13], off
	s_cbranch_vccnz .LBB0_1753
	s_andn2_b64 vcc, exec, s[6:7]
	s_cbranch_vccnz .LBB0_1752
	s_barrier
	s_branch .LBB0_1752
